# v42: v41 + packed v_pk_add_f32 split into scalar add/sub pairs in both attention softmax blocks (94 sites, bit-identical)
# baseline (speedup 1.0000x reference)
.LBB0_1062:
	v_exp_f32_e64 v91, -v90
	v_add_f32_e32 v123, v123, v90
	v_sub_f32_e32 v50, v50, v90
	v_sub_f32_e32 v51, v51, v90
	v_sub_f32_e32 v34, v34, v90
	v_sub_f32_e32 v35, v35, v90
	v_sub_f32_e32 v52, v52, v90
	v_sub_f32_e32 v53, v53, v90
	v_sub_f32_e32 v36, v36, v90
	v_sub_f32_e32 v37, v37, v90
	v_sub_f32_e32 v54, v54, v90
	v_sub_f32_e32 v55, v55, v90
	v_sub_f32_e32 v38, v38, v90
	v_sub_f32_e32 v39, v39, v90
	v_sub_f32_e32 v56, v56, v90
	v_sub_f32_e32 v57, v57, v90
	v_sub_f32_e32 v40, v40, v90
	v_sub_f32_e32 v41, v41, v90
	v_sub_f32_e32 v58, v58, v90
	v_sub_f32_e32 v59, v59, v90
	v_sub_f32_e32 v42, v42, v90
	v_sub_f32_e32 v43, v43, v90
	v_sub_f32_e32 v60, v60, v90
	v_sub_f32_e32 v61, v61, v90
	v_sub_f32_e32 v44, v44, v90
	v_sub_f32_e32 v45, v45, v90
	v_sub_f32_e32 v62, v62, v90
	v_sub_f32_e32 v63, v63, v90
	v_sub_f32_e32 v46, v46, v90
	v_sub_f32_e32 v47, v47, v90
	v_sub_f32_e32 v64, v64, v90
	v_sub_f32_e32 v65, v65, v90
	v_sub_f32_e32 v48, v48, v90
	v_sub_f32_e32 v49, v49, v90
	v_cndmask_b32_e64 v91, v91, 1.0, s[12:13]
	v_cmp_gt_f32_e32 vcc, 1.0, v91
	s_cbranch_vccz .LBB0_1066

.LBB0_1066:
	v_exp_f32_e32 v50, v50
	v_exp_f32_e32 v34, v34
	v_exp_f32_e32 v51, v51
	v_exp_f32_e32 v35, v35
	v_exp_f32_e32 v52, v52
	v_exp_f32_e32 v53, v53
	v_exp_f32_e32 v36, v36
	v_exp_f32_e32 v37, v37
	v_exp_f32_e32 v54, v54
	v_exp_f32_e32 v55, v55
	v_exp_f32_e32 v38, v38
	v_exp_f32_e32 v39, v39
	v_add_f32_e32 v92, v34, v50
	v_add_f32_e32 v93, v35, v51
	v_exp_f32_e32 v56, v56
	v_exp_f32_e32 v57, v57
	v_add_f32_e32 v92, v52, v92
	v_add_f32_e32 v93, v53, v93
	v_exp_f32_e32 v40, v40
	v_exp_f32_e32 v41, v41
	v_add_f32_e32 v92, v36, v92
	v_add_f32_e32 v93, v37, v93
	v_exp_f32_e32 v58, v58
	v_exp_f32_e32 v59, v59
	v_add_f32_e32 v92, v54, v92
	v_add_f32_e32 v93, v55, v93
	v_exp_f32_e32 v42, v42
	v_exp_f32_e32 v43, v43
	v_add_f32_e32 v92, v38, v92
	v_add_f32_e32 v93, v39, v93
	v_exp_f32_e32 v60, v60
	v_exp_f32_e32 v61, v61
	v_add_f32_e32 v92, v56, v92
	v_add_f32_e32 v93, v57, v93
	v_exp_f32_e32 v44, v44
	v_exp_f32_e32 v45, v45
	v_add_f32_e32 v92, v40, v92
	v_add_f32_e32 v93, v41, v93
	v_exp_f32_e32 v62, v62
	v_exp_f32_e32 v63, v63
	v_add_f32_e32 v92, v58, v92
	v_add_f32_e32 v93, v59, v93
	v_exp_f32_e32 v46, v46
	v_exp_f32_e32 v47, v47
	v_add_f32_e32 v92, v42, v92
	v_add_f32_e32 v93, v43, v93
	v_exp_f32_e32 v64, v64
	v_exp_f32_e32 v65, v65
	v_add_f32_e32 v92, v60, v92
	v_add_f32_e32 v93, v61, v93
	v_exp_f32_e32 v48, v48
	v_exp_f32_e32 v49, v49
	v_add_f32_e32 v92, v44, v92
	v_add_f32_e32 v93, v45, v93
	v_cvt_pk_bf16_f32 v90, v50, v51
	v_add_f32_e32 v92, v62, v92
	v_add_f32_e32 v93, v63, v93
	v_cvt_pk_bf16_f32 v94, v58, v59
	v_add_f32_e32 v92, v46, v92
	v_add_f32_e32 v93, v47, v93
	v_cvt_pk_bf16_f32 v95, v60, v61
	v_add_f32_e32 v92, v64, v92
	v_add_f32_e32 v93, v65, v93
	v_cvt_pk_bf16_f32 v96, v62, v63
	v_add_f32_e32 v92, v48, v92
	v_add_f32_e32 v93, v49, v93
	v_cvt_pk_bf16_f32 v97, v64, v65
	v_add_f32_e32 v125, v92, v93
	v_fmac_f32_e32 v125, v124, v91
	v_cvt_pk_bf16_f32 v91, v52, v53
	v_cvt_pk_bf16_f32 v92, v54, v55
	v_cvt_pk_bf16_f32 v93, v56, v57
	v_cvt_pk_bf16_f32 v98, v34, v35
	v_cvt_pk_bf16_f32 v99, v36, v37
	v_cvt_pk_bf16_f32 v100, v38, v39
	v_cvt_pk_bf16_f32 v101, v40, v41
	v_cvt_pk_bf16_f32 v102, v42, v43
	v_cvt_pk_bf16_f32 v103, v44, v45
	v_cvt_pk_bf16_f32 v104, v46, v47
	v_cvt_pk_bf16_f32 v105, v48, v49
	v_permlane32_swap_b32_e32 v90, v92
	v_permlane32_swap_b32_e32 v91, v93
	v_permlane32_swap_b32_e32 v94, v96
	v_permlane32_swap_b32_e32 v95, v97
	v_permlane32_swap_b32_e32 v98, v100
	v_permlane32_swap_b32_e32 v99, v101
	v_permlane32_swap_b32_e32 v102, v104
	v_permlane32_swap_b32_e32 v103, v105
	v_mov_b32_e32 v124, v125
	s_and_b64 vcc, exec, s[6:7]
	s_mov_b64 s[12:13], -1
	s_cbranch_vccz .LBB0_1046

.LBB0_1088:
	s_add_i32 s4, s78, 1
	s_sub_i32 s14, s93, 63
	s_cmp_le_i32 s14, s80
	s_cselect_b64 s[76:77], -1, 0
	s_cmp_gt_i32 s14, s80
	s_cbranch_scc1 .LBB0_1096
	v_cndmask_b32_e64 v0, 0, v195, s[82:83]
	v_sub_f32_e32 v0, v165, v0
	s_xor_b64 s[12:13], s[82:83], -1
	v_sub_f32_e32 v66, v66, v0
	v_sub_f32_e32 v67, v67, v0
	v_sub_f32_e32 v82, v82, v0
	v_sub_f32_e32 v83, v83, v0
	v_sub_f32_e32 v68, v68, v0
	v_sub_f32_e32 v69, v69, v0
	v_sub_f32_e32 v84, v84, v0
	v_sub_f32_e32 v85, v85, v0
	v_sub_f32_e32 v70, v70, v0
	v_sub_f32_e32 v71, v71, v0
	v_sub_f32_e32 v86, v86, v0
	v_sub_f32_e32 v87, v87, v0
	v_sub_f32_e32 v72, v72, v0
	v_sub_f32_e32 v73, v73, v0
	v_sub_f32_e32 v88, v88, v0
	v_sub_f32_e32 v89, v89, v0
	v_sub_f32_e32 v74, v74, v0
	v_sub_f32_e32 v75, v75, v0
	v_sub_f32_e32 v90, v90, v0
	v_sub_f32_e32 v91, v91, v0
	v_sub_f32_e32 v76, v76, v0
	v_sub_f32_e32 v77, v77, v0
	v_sub_f32_e32 v92, v92, v0
	v_sub_f32_e32 v93, v93, v0
	v_sub_f32_e32 v78, v78, v0
	v_sub_f32_e32 v79, v79, v0
	v_sub_f32_e32 v94, v94, v0
	v_sub_f32_e32 v95, v95, v0
	v_sub_f32_e32 v80, v80, v0
	v_sub_f32_e32 v81, v81, v0
	s_andn2_b64 vcc, exec, s[12:13]
	v_sub_f32_e32 v96, v96, v0
	v_sub_f32_e32 v97, v97, v0
	s_cbranch_vccnz .LBB0_1091
	v_mov_b32_e32 v0, v167
	ds_read_b128 v[114:117], v0
	ds_read_b128 v[118:121], v0 offset:128
	ds_read_b128 v[122:125], v0 offset:32
	ds_read_b128 v[126:129], v0 offset:160
	s_waitcnt lgkmcnt(3)
	v_sub_u32_e32 v114, v187, v114
	v_sub_u32_e32 v115, v187, v115
	s_waitcnt lgkmcnt(2)
	v_sub_u32_e32 v118, v187, v118
	v_med3_i32 v114, v114, 0, v241
	v_med3_i32 v115, v115, 0, v241
	v_sub_u32_e32 v119, v187, v119
	v_sub_u32_e32 v116, v187, v116
	v_sub_u32_e32 v120, v187, v120
	v_sub_u32_e32 v117, v187, v117
	v_sub_u32_e32 v121, v187, v121
	v_med3_i32 v118, v118, 0, v241
	v_lshl_add_u32 v114, v114, 2, s92
	v_med3_i32 v119, v119, 0, v241
	v_lshl_add_u32 v115, v115, 2, s92
	v_med3_i32 v116, v116, 0, v241
	v_med3_i32 v120, v120, 0, v241
	v_med3_i32 v117, v117, 0, v241
	v_med3_i32 v121, v121, 0, v241
	v_lshl_add_u32 v118, v118, 2, s92
	v_lshl_add_u32 v119, v119, 2, s92
	v_lshl_add_u32 v116, v116, 2, s92
	v_lshl_add_u32 v120, v120, 2, s92
	v_lshl_add_u32 v117, v117, 2, s92
	v_lshl_add_u32 v121, v121, 2, s92
	ds_read_b32 v200, v114
	ds_read_b32 v202, v118
	ds_read_b32 v201, v115
	ds_read_b32 v203, v119
	ds_read_b32 v204, v116
	ds_read_b32 v206, v120
	ds_read_b32 v205, v117
	ds_read_b32 v207, v121
	s_waitcnt lgkmcnt(9)
	v_sub_u32_e32 v114, v187, v122
	s_waitcnt lgkmcnt(8)
	v_sub_u32_e32 v115, v187, v126
	v_med3_i32 v114, v114, 0, v241
	v_med3_i32 v115, v115, 0, v241
	v_lshl_add_u32 v118, v114, 2, s92
	v_lshl_add_u32 v119, v115, 2, s92
	v_sub_u32_e32 v114, v187, v123
	v_sub_u32_e32 v115, v187, v127
	v_med3_i32 v114, v114, 0, v241
	v_med3_i32 v115, v115, 0, v241
	v_lshl_add_u32 v120, v114, 2, s92
	v_lshl_add_u32 v121, v115, 2, s92
	v_sub_u32_e32 v114, v187, v124
	v_sub_u32_e32 v115, v187, v128
	v_med3_i32 v114, v114, 0, v241
	v_med3_i32 v115, v115, 0, v241
	v_lshl_add_u32 v122, v114, 2, s92
	v_lshl_add_u32 v123, v115, 2, s92
	v_sub_u32_e32 v114, v187, v125
	v_sub_u32_e32 v115, v187, v129
	v_med3_i32 v114, v114, 0, v241
	v_med3_i32 v115, v115, 0, v241
	v_lshl_add_u32 v124, v114, 2, s92
	v_lshl_add_u32 v125, v115, 2, s92
	ds_read_b128 v[114:117], v0 offset:64
	ds_read_b32 v208, v118
	ds_read_b32 v210, v119
	ds_read_b32 v209, v120
	ds_read_b32 v211, v121
	ds_read_b32 v212, v122
	ds_read_b32 v214, v123
	ds_read_b32 v213, v124
	ds_read_b32 v215, v125
	ds_read_b128 v[118:121], v0 offset:192
	ds_read_b128 v[122:125], v0 offset:96
	s_waitcnt lgkmcnt(10)
	v_sub_u32_e32 v116, v187, v116
	v_med3_i32 v116, v116, 0, v241
	v_sub_u32_e32 v114, v187, v114
	ds_read_b128 v[126:129], v0 offset:224
	s_waitcnt lgkmcnt(2)
	v_sub_u32_e32 v0, v187, v118
	v_sub_u32_e32 v115, v187, v115
	v_sub_u32_e32 v118, v187, v119
	v_sub_u32_e32 v119, v187, v120
	v_lshl_add_u32 v120, v116, 2, s92
	v_sub_u32_e32 v116, v187, v117
	v_med3_i32 v114, v114, 0, v241
	v_med3_i32 v115, v115, 0, v241
	v_med3_i32 v118, v118, 0, v241
	v_med3_i32 v119, v119, 0, v241
	v_med3_i32 v116, v116, 0, v241
	v_sub_u32_e32 v117, v187, v121
	v_med3_i32 v0, v0, 0, v241
	v_lshl_add_u32 v114, v114, 2, s92
	v_lshl_add_u32 v115, v115, 2, s92
	v_lshl_add_u32 v118, v118, 2, s92
	v_lshl_add_u32 v119, v119, 2, s92
	v_med3_i32 v117, v117, 0, v241
	v_lshl_add_u32 v121, v116, 2, s92
	v_lshl_add_u32 v0, v0, 2, s92
	v_lshl_add_u32 v173, v117, 2, s92
	ds_read_b32 v114, v114
	ds_read_b32 v116, v0
	ds_read_b32 v115, v115
	ds_read_b32 v117, v118
	ds_read_b32 v118, v120
	ds_read_b32 v120, v119
	ds_read_b32 v119, v121
	ds_read_b32 v121, v173
	s_waitcnt lgkmcnt(9)
	v_sub_u32_e32 v0, v187, v122
	s_waitcnt lgkmcnt(8)
	v_sub_u32_e32 v122, v187, v126
	v_sub_u32_e32 v123, v187, v123
	v_sub_u32_e32 v126, v187, v127
	v_sub_u32_e32 v124, v187, v124
	v_sub_u32_e32 v127, v187, v128
	v_sub_u32_e32 v125, v187, v125
	v_sub_u32_e32 v128, v187, v129
	v_med3_i32 v0, v0, 0, v241
	v_med3_i32 v122, v122, 0, v241
	v_med3_i32 v123, v123, 0, v241
	v_med3_i32 v124, v124, 0, v241
	v_med3_i32 v125, v125, 0, v241
	v_med3_i32 v128, v128, 0, v241
	v_lshl_add_u32 v0, v0, 2, s92
	v_lshl_add_u32 v122, v122, 2, s92
	v_med3_i32 v126, v126, 0, v241
	v_lshl_add_u32 v123, v123, 2, s92
	v_med3_i32 v127, v127, 0, v241
	v_lshl_add_u32 v124, v124, 2, s92
	v_lshl_add_u32 v125, v125, 2, s92
	s_waitcnt lgkmcnt(1)
	v_add_f32_e32 v76, v76, v118
	v_add_f32_e32 v77, v77, v119
	v_lshl_add_u32 v119, v128, 2, s92
	v_lshl_add_u32 v126, v126, 2, s92
	v_lshl_add_u32 v127, v127, 2, s92
	v_add_f32_e32 v74, v74, v114
	v_add_f32_e32 v75, v75, v115
	ds_read_b32 v114, v0
	ds_read_b32 v118, v122
	ds_read_b32 v115, v123
	ds_read_b32 v122, v124
	ds_read_b32 v123, v125
	ds_read_b32 v125, v119
	ds_read_b32 v124, v127
	ds_read_b32 v119, v126
	v_add_f32_e32 v66, v66, v200
	v_add_f32_e32 v67, v67, v201
	v_add_f32_e32 v68, v68, v204
	v_add_f32_e32 v69, v69, v205
	v_add_f32_e32 v70, v70, v208
	v_add_f32_e32 v71, v71, v209
	v_add_f32_e32 v72, v72, v212
	v_add_f32_e32 v73, v73, v213
	s_waitcnt lgkmcnt(5)
	v_add_f32_e32 v78, v78, v114
	v_add_f32_e32 v79, v79, v115
	s_waitcnt lgkmcnt(3)
	v_add_f32_e32 v80, v80, v122
	v_add_f32_e32 v81, v81, v123
	v_add_f32_e32 v82, v82, v202
	v_add_f32_e32 v83, v83, v203
	v_add_f32_e32 v84, v84, v206
	v_add_f32_e32 v85, v85, v207
	v_add_f32_e32 v86, v86, v210
	v_add_f32_e32 v87, v87, v211
	v_add_f32_e32 v88, v88, v214
	v_add_f32_e32 v89, v89, v215
	v_add_f32_e32 v90, v90, v116
	v_add_f32_e32 v91, v91, v117
	v_add_f32_e32 v92, v92, v120
	v_add_f32_e32 v93, v93, v121
	s_waitcnt lgkmcnt(0)
	v_add_f32_e32 v94, v94, v118
	v_add_f32_e32 v95, v95, v119
	v_add_f32_e32 v96, v96, v124
	v_add_f32_e32 v97, v97, v125

.LBB0_1113:
	v_exp_f32_e64 v114, -v0
	v_sub_f32_e32 v66, v66, v0
	v_sub_f32_e32 v67, v67, v0
	v_sub_f32_e32 v82, v82, v0
	v_sub_f32_e32 v83, v83, v0
	v_sub_f32_e32 v68, v68, v0
	v_sub_f32_e32 v69, v69, v0
	v_sub_f32_e32 v84, v84, v0
	v_sub_f32_e32 v85, v85, v0
	v_sub_f32_e32 v70, v70, v0
	v_sub_f32_e32 v71, v71, v0
	v_sub_f32_e32 v86, v86, v0
	v_sub_f32_e32 v87, v87, v0
	v_sub_f32_e32 v72, v72, v0
	v_sub_f32_e32 v73, v73, v0
	v_sub_f32_e32 v88, v88, v0
	v_sub_f32_e32 v89, v89, v0
	v_sub_f32_e32 v74, v74, v0
	v_sub_f32_e32 v75, v75, v0
	v_sub_f32_e32 v90, v90, v0
	v_sub_f32_e32 v91, v91, v0
	v_sub_f32_e32 v76, v76, v0
	v_sub_f32_e32 v77, v77, v0
	v_sub_f32_e32 v92, v92, v0
	v_sub_f32_e32 v93, v93, v0
	v_sub_f32_e32 v78, v78, v0
	v_sub_f32_e32 v79, v79, v0
	v_sub_f32_e32 v94, v94, v0
	v_sub_f32_e32 v95, v95, v0
	v_sub_f32_e32 v80, v80, v0
	v_sub_f32_e32 v81, v81, v0
	v_sub_f32_e32 v96, v96, v0
	v_sub_f32_e32 v97, v97, v0
	v_add_f32_e32 v165, v165, v0
	v_cndmask_b32_e64 v114, v114, 1.0, s[12:13]
	v_cmp_gt_f32_e32 vcc, 1.0, v114
	s_cbranch_vccz .LBB0_1117

.LBB0_1117:
	v_exp_f32_e32 v66, v66
	v_exp_f32_e32 v82, v82
	v_exp_f32_e32 v67, v67
	v_exp_f32_e32 v83, v83
	v_exp_f32_e32 v68, v68
	v_exp_f32_e32 v69, v69
	v_exp_f32_e32 v84, v84
	v_exp_f32_e32 v85, v85
	v_exp_f32_e32 v70, v70
	v_exp_f32_e32 v71, v71
	v_exp_f32_e32 v86, v86
	v_exp_f32_e32 v87, v87
	v_add_f32_e32 v116, v82, v66
	v_add_f32_e32 v117, v83, v67
	v_exp_f32_e32 v72, v72
	v_exp_f32_e32 v73, v73
	v_add_f32_e32 v116, v68, v116
	v_add_f32_e32 v117, v69, v117
	v_exp_f32_e32 v88, v88
	v_exp_f32_e32 v89, v89
	v_add_f32_e32 v116, v84, v116
	v_add_f32_e32 v117, v85, v117
	v_exp_f32_e32 v74, v74
	v_exp_f32_e32 v75, v75
	v_add_f32_e32 v116, v70, v116
	v_add_f32_e32 v117, v71, v117
	v_exp_f32_e32 v90, v90
	v_exp_f32_e32 v91, v91
	v_add_f32_e32 v116, v86, v116
	v_add_f32_e32 v117, v87, v117
	v_exp_f32_e32 v76, v76
	v_exp_f32_e32 v77, v77
	v_add_f32_e32 v116, v72, v116
	v_add_f32_e32 v117, v73, v117
	v_exp_f32_e32 v92, v92
	v_exp_f32_e32 v93, v93
	v_add_f32_e32 v116, v88, v116
	v_add_f32_e32 v117, v89, v117
	v_exp_f32_e32 v78, v78
	v_exp_f32_e32 v79, v79
	v_add_f32_e32 v116, v74, v116
	v_add_f32_e32 v117, v75, v117
	v_exp_f32_e32 v94, v94
	v_exp_f32_e32 v95, v95
	v_add_f32_e32 v116, v90, v116
	v_add_f32_e32 v117, v91, v117
	v_exp_f32_e32 v80, v80
	v_exp_f32_e32 v81, v81
	v_add_f32_e32 v116, v76, v116
	v_add_f32_e32 v117, v77, v117
	v_exp_f32_e32 v96, v96
	v_exp_f32_e32 v97, v97
	v_add_f32_e32 v116, v92, v116
	v_add_f32_e32 v117, v93, v117
	v_cvt_pk_bf16_f32 v115, v68, v69
	v_add_f32_e32 v116, v78, v116
	v_add_f32_e32 v117, v79, v117
	v_cvt_pk_bf16_f32 v118, v74, v75
	v_add_f32_e32 v116, v94, v116
	v_add_f32_e32 v117, v95, v117
	v_cvt_pk_bf16_f32 v119, v76, v77
	v_add_f32_e32 v116, v80, v116
	v_add_f32_e32 v117, v81, v117
	v_cvt_pk_bf16_f32 v120, v78, v79
	v_add_f32_e32 v116, v96, v116
	v_add_f32_e32 v117, v97, v117
	v_cvt_pk_bf16_f32 v121, v80, v81
	v_add_f32_e32 v0, v116, v117
	v_fmac_f32_e32 v0, v171, v114
	v_cvt_pk_bf16_f32 v114, v66, v67
	v_cvt_pk_bf16_f32 v116, v70, v71
	v_cvt_pk_bf16_f32 v117, v72, v73
	v_cvt_pk_bf16_f32 v122, v82, v83
	v_cvt_pk_bf16_f32 v123, v84, v85
	v_cvt_pk_bf16_f32 v124, v86, v87
	v_cvt_pk_bf16_f32 v125, v88, v89
	v_cvt_pk_bf16_f32 v126, v90, v91
	v_cvt_pk_bf16_f32 v127, v92, v93
	v_cvt_pk_bf16_f32 v128, v94, v95
	v_cvt_pk_bf16_f32 v129, v96, v97
	v_permlane32_swap_b32_e32 v114, v116
	v_permlane32_swap_b32_e32 v115, v117
	v_permlane32_swap_b32_e32 v118, v120
	v_permlane32_swap_b32_e32 v119, v121
	v_permlane32_swap_b32_e32 v122, v124
	v_permlane32_swap_b32_e32 v123, v125
	v_permlane32_swap_b32_e32 v126, v128
	v_permlane32_swap_b32_e32 v127, v129
	v_mov_b32_e32 v171, v0
	s_and_b64 vcc, exec, s[6:7]
	s_mov_b64 s[12:13], -1
	s_cbranch_vccz .LBB0_1097
